# Y2 (GEMM2 output) stored plain again as well; only Z stays write-through
# speedup vs baseline: 1.0178x; 1.0099x over previous
;     __device__ __forceinline__ void operator()() { if (cnt == turn) run_all(tid_); ++cnt; }
;     __device__ __forceinline__ void operator()(const Acc& acc, const Unit& u, int wr, int wc, int fr, int fq) const {
;         const int row0 = u.pm * BM + wr * 64 + fr, col0 = u.pn * BM + wc * 32 + 8 * fq;
;         f16* Og = O + (size_t)u.g * EROWS * DM;
; #pragma unroll
;         for (int ai = 0; ai < 2; ++ai)
; #pragma unroll
;             for (int m = 0; m < 4; ++m) { const int row = row0 + ai * HALF + m * 16; const float s = gv[((row >> 8) * NE + u.g) * CAP + (row & 255)];
;                 f16* rowp = Og + (size_t)row * DM + col0;
; #pragma unroll
;                 for (int bj = 0; bj < 2; ++bj) { const f32x4 v0 = acc[ai][bj][m][0] * s, v1 = acc[ai][bj][m][1] * s;
;                     u32x4 w; w.x = pkh(v0[0], v0[1]); w.y = pkh(v0[2], v0[3]); w.z = pkh(v1[0], v1[1]); w.w = pkh(v1[2], v1[3]);
;                     *(u32x4*)(rowp + bj * HALF) = w; } }
;     }
.LBB0_1105:
	v_lshl_add_u32 v148, s48, 8, v1
	v_lshrrev_b32_e32 v146, 4, v148
	v_and_b32_e32 v146, 0xfffff0, v146
	v_add_lshl_u32 v166, v146, s18, 8
	v_or_b32_e32 v146, v166, v151
	v_ashrrev_i32_e32 v147, 31, v146
	v_lshl_add_u64 v[146:147], v[146:147], 2, s[72:73]
	global_load_dword v226, v[146:147], off
	global_load_dword v227, v[146:147], off offset:64
	global_load_dword v228, v[146:147], off offset:128
	global_load_dword v229, v[146:147], off offset:192
	global_load_dword v230, v[146:147], off offset:512
	global_load_dword v231, v[146:147], off offset:576
	global_load_dword v232, v[146:147], off offset:640
	global_load_dword v233, v[146:147], off offset:704
	v_lshl_or_b32 v146, s19, 8, v152
	s_ashr_i32 s19, s18, 31
	s_lshl_b64 s[2:3], s[18:19], 23
	s_add_u32 s2, s74, s2
	v_ashrrev_i32_e32 v147, 31, v146
	v_ashrrev_i32_e32 v149, 31, v148
	v_or_b32_e32 v158, 16, v148
	s_addc_u32 s3, s75, s3
	v_lshlrev_b64 v[160:161], 11, v[148:149]
	v_lshl_add_u64 v[146:147], v[146:147], 1, s[2:3]
	v_and_or_b32 v162, v158, s44, v166
	v_lshl_add_u64 v[160:161], v[146:147], 0, v[160:161]
	v_ashrrev_i32_e32 v163, 31, v162
	v_lshl_add_u64 v[162:163], v[162:163], 2, s[72:73]
	v_ashrrev_i32_e32 v159, 31, v158
	s_movk_i32 s2, 0xcf
	s_and_b64 vcc, exec, s[4:5]
	s_waitcnt vmcnt(0)
	v_mov_b32_e32 v156, v226
	v_pk_mul_f32 v[128:129], v[128:129], v[156:157] op_sel_hi:[1,0]
	v_pk_mul_f32 v[126:127], v[126:127], v[156:157] op_sel_hi:[1,0]
	v_pk_mul_f32 v[124:125], v[124:125], v[156:157] op_sel_hi:[1,0]
	v_pk_mul_f32 v[122:123], v[122:123], v[156:157] op_sel_hi:[1,0]
	v_pk_mul_f32 v[120:121], v[120:121], v[156:157] op_sel_hi:[1,0]
	v_pk_mul_f32 v[118:119], v[118:119], v[156:157] op_sel_hi:[1,0]
	v_pk_mul_f32 v[164:165], v[116:117], v[156:157] op_sel_hi:[1,0]
	v_pk_mul_f32 v[156:157], v[114:115], v[156:157] op_sel_hi:[1,0]
	v_cvt_pk_f16_f32 v114, v126, v127
	v_cvt_pk_f16_f32 v115, v128, v129
	v_cvt_pk_f16_f32 v116, v122, v123
	v_cvt_pk_f16_f32 v117, v124, v125
	v_cvt_pk_f16_f32 v118, v118, v119
	v_cvt_pk_f16_f32 v119, v120, v121
	v_cvt_pk_f16_f32 v120, v156, v157
	v_cvt_pk_f16_f32 v121, v164, v165
	global_store_dwordx4 v[160:161], v[114:117], off
	global_store_dwordx4 v[160:161], v[118:121], off offset:256
	s_nop 0
	v_or_b32_e32 v116, 32, v148
	v_lshlrev_b64 v[118:119], 11, v[158:159]
	v_and_or_b32 v120, v116, s45, v166
	v_lshl_add_u64 v[118:119], v[146:147], 0, v[118:119]
	v_ashrrev_i32_e32 v121, 31, v120
	v_lshl_add_u64 v[120:121], v[120:121], 2, s[72:73]
	v_ashrrev_i32_e32 v117, 31, v116
	s_nop 0
	v_mov_b32_e32 v114, v227
	v_pk_mul_f32 v[112:113], v[112:113], v[114:115] op_sel_hi:[1,0]
	v_pk_mul_f32 v[110:111], v[110:111], v[114:115] op_sel_hi:[1,0]
	v_pk_mul_f32 v[108:109], v[108:109], v[114:115] op_sel_hi:[1,0]
	v_pk_mul_f32 v[106:107], v[106:107], v[114:115] op_sel_hi:[1,0]
	v_pk_mul_f32 v[104:105], v[104:105], v[114:115] op_sel_hi:[1,0]
	v_pk_mul_f32 v[102:103], v[102:103], v[114:115] op_sel_hi:[1,0]
	v_pk_mul_f32 v[122:123], v[100:101], v[114:115] op_sel_hi:[1,0]
	v_pk_mul_f32 v[114:115], v[98:99], v[114:115] op_sel_hi:[1,0]
	v_cvt_pk_f16_f32 v98, v110, v111
	v_cvt_pk_f16_f32 v99, v112, v113
	v_cvt_pk_f16_f32 v100, v106, v107
	v_cvt_pk_f16_f32 v101, v108, v109
	v_cvt_pk_f16_f32 v102, v102, v103
	v_cvt_pk_f16_f32 v103, v104, v105
	v_cvt_pk_f16_f32 v104, v114, v115
	v_cvt_pk_f16_f32 v105, v122, v123
	global_store_dwordx4 v[118:119], v[98:101], off
	global_store_dwordx4 v[118:119], v[102:105], off offset:256
	s_nop 0
	v_or_b32_e32 v100, 48, v148
	v_lshlrev_b64 v[102:103], 11, v[116:117]
	v_and_or_b32 v104, v100, s46, v166
	v_lshl_add_u64 v[102:103], v[146:147], 0, v[102:103]
	v_ashrrev_i32_e32 v105, 31, v104
	v_lshl_add_u64 v[104:105], v[104:105], 2, s[72:73]
	v_ashrrev_i32_e32 v101, 31, v100
	s_nop 0
	v_mov_b32_e32 v98, v228
	v_pk_mul_f32 v[96:97], v[96:97], v[98:99] op_sel_hi:[1,0]
	v_pk_mul_f32 v[94:95], v[94:95], v[98:99] op_sel_hi:[1,0]
	v_pk_mul_f32 v[92:93], v[92:93], v[98:99] op_sel_hi:[1,0]
	v_pk_mul_f32 v[90:91], v[90:91], v[98:99] op_sel_hi:[1,0]
	v_pk_mul_f32 v[88:89], v[88:89], v[98:99] op_sel_hi:[1,0]
	v_pk_mul_f32 v[86:87], v[86:87], v[98:99] op_sel_hi:[1,0]
	v_pk_mul_f32 v[106:107], v[84:85], v[98:99] op_sel_hi:[1,0]
	v_pk_mul_f32 v[98:99], v[82:83], v[98:99] op_sel_hi:[1,0]
	v_cvt_pk_f16_f32 v82, v94, v95
	v_cvt_pk_f16_f32 v83, v96, v97
	v_cvt_pk_f16_f32 v84, v90, v91
	v_cvt_pk_f16_f32 v85, v92, v93
	v_cvt_pk_f16_f32 v86, v86, v87
	v_cvt_pk_f16_f32 v87, v88, v89
	v_cvt_pk_f16_f32 v88, v98, v99
	v_cvt_pk_f16_f32 v89, v106, v107
	global_store_dwordx4 v[102:103], v[82:85], off
	global_store_dwordx4 v[102:103], v[86:89], off offset:256
	s_nop 0
	v_add_u32_e32 v84, 0x80, v148
	v_lshrrev_b32_e32 v83, 4, v84
	v_and_b32_e32 v83, 0xfffff0, v83
	v_add_lshl_u32 v92, v83, s18, 8
	v_lshlrev_b64 v[86:87], 11, v[100:101]
	v_and_or_b32 v88, v84, s2, v92
	v_lshl_add_u64 v[86:87], v[146:147], 0, v[86:87]
	v_ashrrev_i32_e32 v89, 31, v88
	v_lshl_add_u64 v[88:89], v[88:89], 2, s[72:73]
	v_ashrrev_i32_e32 v85, 31, v84
	s_mov_b64 s[2:3], -1
	s_nop 0
	v_mov_b32_e32 v82, v229
	v_pk_mul_f32 v[80:81], v[80:81], v[82:83] op_sel_hi:[1,0]
	v_pk_mul_f32 v[78:79], v[78:79], v[82:83] op_sel_hi:[1,0]
; #define GM_BAR __builtin_amdgcn_s_barrier()
;     __device__ __forceinline__ void operator()(const Acc& acc, const Unit& u, int wr, int wc, int fr, int fq) const {
;     ...
;             for (int m = 0; m < 4; ++m) { const int row = row0 + ai * HALF + m * 16; const float s = gv[((row >> 8) * NE + u.g) * CAP + (row & 255)];
;                 f16* rowp = Og + (size_t)row * DM + col0;
; #pragma unroll
;                 for (int bj = 0; bj < 2; ++bj) { const f32x4 v0 = acc[ai][bj][m][0] * s, v1 = acc[ai][bj][m][1] * s;
;                     u32x4 w; w.x = pkh(v0[0], v0[1]); w.y = pkh(v0[2], v0[3]); w.z = pkh(v1[0], v1[1]); w.w = pkh(v1[2], v1[3]);
;                     *(u32x4*)(rowp + bj * HALF) = w; } }
; template <bool BF, bool GATHER = false, class Epi, class Hook>
; __device__ __forceinline__ void gemm_phase(LAS unsigned char* lds, const Gemm g, const Order& S, const Epi& E, Hook& HK) {
;     ...
;         if (!has_next) break;
; #pragma unroll
;         for (int a = 0; a < 2; ++a)
; #pragma unroll
;             for (int b = 0; b < 2; ++b)
; #pragma unroll
;                 for (int m = 0; m < 4; ++m)
; #pragma unroll
;                     for (int n = 0; n < 2; ++n) acc[a][b][m][n] = (f32x4){0.f, 0.f, 0.f, 0.f};
;         cur = nxt; cA = nA; cB = nB; ++ui;
;         if constexpr (GATHER) { gA0[0] = nA0[0]; gA0[1] = nA0[1]; gA1[0] = nA1[0]; gA1[1] = nA1[1]; }
;         if (wr == 1) GM_BAR;
	v_pk_mul_f32 v[76:77], v[76:77], v[82:83] op_sel_hi:[1,0]
	v_pk_mul_f32 v[74:75], v[74:75], v[82:83] op_sel_hi:[1,0]
	v_pk_mul_f32 v[72:73], v[72:73], v[82:83] op_sel_hi:[1,0]
	v_pk_mul_f32 v[70:71], v[70:71], v[82:83] op_sel_hi:[1,0]
	v_pk_mul_f32 v[90:91], v[68:69], v[82:83] op_sel_hi:[1,0]
	v_pk_mul_f32 v[82:83], v[66:67], v[82:83] op_sel_hi:[1,0]
	v_cvt_pk_f16_f32 v66, v78, v79
	v_cvt_pk_f16_f32 v67, v80, v81
	v_cvt_pk_f16_f32 v68, v74, v75
	v_cvt_pk_f16_f32 v69, v76, v77
	v_cvt_pk_f16_f32 v70, v70, v71
	v_cvt_pk_f16_f32 v71, v72, v73
	v_cvt_pk_f16_f32 v72, v82, v83
	v_cvt_pk_f16_f32 v73, v90, v91
	global_store_dwordx4 v[86:87], v[66:69], off
	global_store_dwordx4 v[86:87], v[70:73], off offset:256
	s_nop 0
	v_add_u32_e32 v68, 0x90, v148
	v_lshlrev_b64 v[70:71], 11, v[84:85]
	v_and_or_b32 v72, v68, s44, v92
	v_lshl_add_u64 v[70:71], v[146:147], 0, v[70:71]
	v_ashrrev_i32_e32 v73, 31, v72
	v_lshl_add_u64 v[72:73], v[72:73], 2, s[72:73]
	v_ashrrev_i32_e32 v69, 31, v68
	s_nop 0
	v_mov_b32_e32 v66, v230
	v_pk_mul_f32 v[64:65], v[64:65], v[66:67] op_sel_hi:[1,0]
	v_pk_mul_f32 v[62:63], v[62:63], v[66:67] op_sel_hi:[1,0]
	v_pk_mul_f32 v[60:61], v[60:61], v[66:67] op_sel_hi:[1,0]
	v_pk_mul_f32 v[58:59], v[58:59], v[66:67] op_sel_hi:[1,0]
	v_pk_mul_f32 v[56:57], v[56:57], v[66:67] op_sel_hi:[1,0]
	v_pk_mul_f32 v[54:55], v[54:55], v[66:67] op_sel_hi:[1,0]
	v_pk_mul_f32 v[74:75], v[52:53], v[66:67] op_sel_hi:[1,0]
	v_pk_mul_f32 v[66:67], v[50:51], v[66:67] op_sel_hi:[1,0]
	v_cvt_pk_f16_f32 v50, v62, v63
	v_cvt_pk_f16_f32 v51, v64, v65
	v_cvt_pk_f16_f32 v52, v58, v59
	v_cvt_pk_f16_f32 v53, v60, v61
	v_cvt_pk_f16_f32 v54, v54, v55
	v_cvt_pk_f16_f32 v55, v56, v57
	v_cvt_pk_f16_f32 v56, v66, v67
	v_cvt_pk_f16_f32 v57, v74, v75
	global_store_dwordx4 v[70:71], v[50:53], off
	global_store_dwordx4 v[70:71], v[54:57], off offset:256
	s_nop 0
	v_add_u32_e32 v52, 0xa0, v148
	v_lshlrev_b64 v[54:55], 11, v[68:69]
	v_and_or_b32 v56, v52, s45, v92
	v_lshl_add_u64 v[54:55], v[146:147], 0, v[54:55]
	v_ashrrev_i32_e32 v57, 31, v56
	v_lshl_add_u64 v[56:57], v[56:57], 2, s[72:73]
	v_ashrrev_i32_e32 v53, 31, v52
	s_nop 0
	v_mov_b32_e32 v50, v231
	v_pk_mul_f32 v[48:49], v[48:49], v[50:51] op_sel_hi:[1,0]
	v_pk_mul_f32 v[46:47], v[46:47], v[50:51] op_sel_hi:[1,0]
	v_pk_mul_f32 v[44:45], v[44:45], v[50:51] op_sel_hi:[1,0]
	v_pk_mul_f32 v[42:43], v[42:43], v[50:51] op_sel_hi:[1,0]
	v_pk_mul_f32 v[40:41], v[40:41], v[50:51] op_sel_hi:[1,0]
	v_pk_mul_f32 v[38:39], v[38:39], v[50:51] op_sel_hi:[1,0]
	v_pk_mul_f32 v[58:59], v[36:37], v[50:51] op_sel_hi:[1,0]
	v_pk_mul_f32 v[50:51], v[34:35], v[50:51] op_sel_hi:[1,0]
	v_cvt_pk_f16_f32 v34, v46, v47
	v_cvt_pk_f16_f32 v35, v48, v49
	v_cvt_pk_f16_f32 v36, v42, v43
	v_cvt_pk_f16_f32 v37, v44, v45
	v_cvt_pk_f16_f32 v38, v38, v39
	v_cvt_pk_f16_f32 v39, v40, v41
	v_cvt_pk_f16_f32 v40, v50, v51
	v_cvt_pk_f16_f32 v41, v58, v59
	global_store_dwordx4 v[54:55], v[34:37], off
	global_store_dwordx4 v[54:55], v[38:41], off offset:256
	s_nop 0
	v_add_u32_e32 v36, 0xb0, v148
	v_lshlrev_b64 v[38:39], 11, v[52:53]
	v_and_or_b32 v40, v36, s46, v92
	v_lshl_add_u64 v[38:39], v[146:147], 0, v[38:39]
	v_ashrrev_i32_e32 v41, 31, v40
	v_lshl_add_u64 v[40:41], v[40:41], 2, s[72:73]
	v_ashrrev_i32_e32 v37, 31, v36
	s_nop 0
	v_mov_b32_e32 v34, v232
	v_pk_mul_f32 v[32:33], v[32:33], v[34:35] op_sel_hi:[1,0]
	v_pk_mul_f32 v[30:31], v[30:31], v[34:35] op_sel_hi:[1,0]
	v_pk_mul_f32 v[28:29], v[28:29], v[34:35] op_sel_hi:[1,0]
	v_pk_mul_f32 v[26:27], v[26:27], v[34:35] op_sel_hi:[1,0]
	v_pk_mul_f32 v[24:25], v[24:25], v[34:35] op_sel_hi:[1,0]
	v_pk_mul_f32 v[22:23], v[22:23], v[34:35] op_sel_hi:[1,0]
	v_pk_mul_f32 v[42:43], v[20:21], v[34:35] op_sel_hi:[1,0]
	v_pk_mul_f32 v[34:35], v[18:19], v[34:35] op_sel_hi:[1,0]
	v_cvt_pk_f16_f32 v18, v30, v31
	v_cvt_pk_f16_f32 v19, v32, v33
	v_cvt_pk_f16_f32 v20, v26, v27
	v_cvt_pk_f16_f32 v21, v28, v29
	v_cvt_pk_f16_f32 v22, v22, v23
	v_cvt_pk_f16_f32 v23, v24, v25
	v_cvt_pk_f16_f32 v24, v34, v35
	v_cvt_pk_f16_f32 v25, v42, v43
	global_store_dwordx4 v[38:39], v[18:21], off
	global_store_dwordx4 v[38:39], v[22:25], off offset:256
	s_nop 0
	v_lshlrev_b64 v[20:21], 11, v[36:37]
	v_lshl_add_u64 v[20:21], v[146:147], 0, v[20:21]
	s_nop 0
	v_mov_b32_e32 v18, v233
	v_pk_mul_f32 v[16:17], v[16:17], v[18:19] op_sel_hi:[1,0]
	v_pk_mul_f32 v[14:15], v[14:15], v[18:19] op_sel_hi:[1,0]
	v_pk_mul_f32 v[12:13], v[12:13], v[18:19] op_sel_hi:[1,0]
	v_pk_mul_f32 v[10:11], v[10:11], v[18:19] op_sel_hi:[1,0]
	v_pk_mul_f32 v[8:9], v[8:9], v[18:19] op_sel_hi:[1,0]
	v_pk_mul_f32 v[6:7], v[6:7], v[18:19] op_sel_hi:[1,0]
	v_pk_mul_f32 v[22:23], v[4:5], v[18:19] op_sel_hi:[1,0]
	v_pk_mul_f32 v[18:19], v[2:3], v[18:19] op_sel_hi:[1,0]
	v_cvt_pk_f16_f32 v2, v14, v15
	v_cvt_pk_f16_f32 v3, v16, v17
	v_cvt_pk_f16_f32 v4, v10, v11
	v_cvt_pk_f16_f32 v5, v12, v13
	v_cvt_pk_f16_f32 v6, v6, v7
	v_cvt_pk_f16_f32 v7, v8, v9
	v_cvt_pk_f16_f32 v8, v18, v19
	v_cvt_pk_f16_f32 v9, v22, v23
	global_store_dwordx4 v[20:21], v[2:5], off
	global_store_dwordx4 v[20:21], v[6:9], off offset:256
	s_cbranch_vccnz .LBB0_1087
	s_andn2_b64 vcc, exec, s[10:11]
	s_cbranch_vccnz .LBB0_1086
	s_barrier
	s_branch .LBB0_1086

;     __device__ __forceinline__ void operator()() { if (cnt == turn) run_all(tid_); ++cnt; }
;     __device__ __forceinline__ void operator()(const Acc& acc, const Unit& u, int wr, int wc, int fr, int fq) const {
;         const int row0 = u.pm * BM + wr * 64 + fr, col0 = u.pn * BM + wc * 32 + 8 * fq;
;         f16* Og = O + (size_t)u.g * EROWS * DM;
; #pragma unroll
;         for (int ai = 0; ai < 2; ++ai)
; #pragma unroll
;             for (int m = 0; m < 4; ++m) { const int row = row0 + ai * HALF + m * 16; const float s = gv[((row >> 8) * NE + u.g) * CAP + (row & 255)];
;                 f16* rowp = Og + (size_t)row * DM + col0;
; #pragma unroll
;                 for (int bj = 0; bj < 2; ++bj) { const f32x4 v0 = acc[ai][bj][m][0] * s, v1 = acc[ai][bj][m][1] * s;
;                     u32x4 w; w.x = pkh(v0[0], v0[1]); w.y = pkh(v0[2], v0[3]); w.z = pkh(v1[0], v1[1]); w.w = pkh(v1[2], v1[3]);
;                     *(u32x4*)(rowp + bj * HALF) = w; } }
;     }
.LBB0_1870:
	v_lshl_add_u32 v148, s49, 8, v1
	v_lshrrev_b32_e32 v146, 4, v148
	v_and_b32_e32 v146, 0xfffff0, v146
	v_add_lshl_u32 v166, v146, s16, 8
	v_or_b32_e32 v146, v166, v151
	v_ashrrev_i32_e32 v147, 31, v146
	v_lshl_add_u64 v[146:147], v[146:147], 2, s[72:73]
	global_load_dword v226, v[146:147], off
	global_load_dword v227, v[146:147], off offset:64
	global_load_dword v228, v[146:147], off offset:128
	global_load_dword v229, v[146:147], off offset:192
	global_load_dword v230, v[146:147], off offset:512
	global_load_dword v231, v[146:147], off offset:576
	global_load_dword v232, v[146:147], off offset:640
	global_load_dword v233, v[146:147], off offset:704
	v_lshl_or_b32 v146, s17, 8, v152
	s_ashr_i32 s17, s16, 31
	s_lshl_b64 s[2:3], s[16:17], 23
	s_add_u32 s2, s74, s2
	v_ashrrev_i32_e32 v147, 31, v146
	v_ashrrev_i32_e32 v149, 31, v148
	v_or_b32_e32 v158, 16, v148
	s_addc_u32 s3, s75, s3
	v_lshlrev_b64 v[160:161], 11, v[148:149]
	v_lshl_add_u64 v[146:147], v[146:147], 1, s[2:3]
	v_and_or_b32 v162, v158, s45, v166
	v_lshl_add_u64 v[160:161], v[146:147], 0, v[160:161]
	v_ashrrev_i32_e32 v163, 31, v162
	v_lshl_add_u64 v[162:163], v[162:163], 2, s[72:73]
	v_ashrrev_i32_e32 v159, 31, v158
	s_and_b64 vcc, exec, s[4:5]
	s_mov_b64 s[2:3], -1
	s_waitcnt vmcnt(0)
	v_mov_b32_e32 v156, v226
	v_pk_mul_f32 v[128:129], v[128:129], v[156:157] op_sel_hi:[1,0]
	v_pk_mul_f32 v[126:127], v[126:127], v[156:157] op_sel_hi:[1,0]
	v_pk_mul_f32 v[124:125], v[124:125], v[156:157] op_sel_hi:[1,0]
	v_pk_mul_f32 v[122:123], v[122:123], v[156:157] op_sel_hi:[1,0]
	v_pk_mul_f32 v[120:121], v[120:121], v[156:157] op_sel_hi:[1,0]
	v_pk_mul_f32 v[118:119], v[118:119], v[156:157] op_sel_hi:[1,0]
	v_pk_mul_f32 v[164:165], v[116:117], v[156:157] op_sel_hi:[1,0]
	v_pk_mul_f32 v[156:157], v[114:115], v[156:157] op_sel_hi:[1,0]
	v_cvt_pk_f16_f32 v114, v126, v127
	v_cvt_pk_f16_f32 v115, v128, v129
	v_cvt_pk_f16_f32 v116, v122, v123
	v_cvt_pk_f16_f32 v117, v124, v125
	v_cvt_pk_f16_f32 v118, v118, v119
	v_cvt_pk_f16_f32 v119, v120, v121
	v_cvt_pk_f16_f32 v120, v156, v157
	v_cvt_pk_f16_f32 v121, v164, v165
	global_store_dwordx4 v[160:161], v[114:117], off
	global_store_dwordx4 v[160:161], v[118:121], off offset:256
	s_nop 0
	v_or_b32_e32 v116, 32, v148
	v_lshlrev_b64 v[118:119], 11, v[158:159]
	v_and_or_b32 v120, v116, s46, v166
	v_lshl_add_u64 v[118:119], v[146:147], 0, v[118:119]
	v_ashrrev_i32_e32 v121, 31, v120
	v_lshl_add_u64 v[120:121], v[120:121], 2, s[72:73]
	v_ashrrev_i32_e32 v117, 31, v116
	s_nop 0
	v_mov_b32_e32 v114, v227
	v_pk_mul_f32 v[112:113], v[112:113], v[114:115] op_sel_hi:[1,0]
	v_pk_mul_f32 v[110:111], v[110:111], v[114:115] op_sel_hi:[1,0]
	v_pk_mul_f32 v[108:109], v[108:109], v[114:115] op_sel_hi:[1,0]
	v_pk_mul_f32 v[106:107], v[106:107], v[114:115] op_sel_hi:[1,0]
	v_pk_mul_f32 v[104:105], v[104:105], v[114:115] op_sel_hi:[1,0]
	v_pk_mul_f32 v[102:103], v[102:103], v[114:115] op_sel_hi:[1,0]
	v_pk_mul_f32 v[122:123], v[100:101], v[114:115] op_sel_hi:[1,0]
	v_pk_mul_f32 v[114:115], v[98:99], v[114:115] op_sel_hi:[1,0]
	v_cvt_pk_f16_f32 v98, v110, v111
	v_cvt_pk_f16_f32 v99, v112, v113
	v_cvt_pk_f16_f32 v100, v106, v107
	v_cvt_pk_f16_f32 v101, v108, v109
	v_cvt_pk_f16_f32 v102, v102, v103
	v_cvt_pk_f16_f32 v103, v104, v105
	v_cvt_pk_f16_f32 v104, v114, v115
	v_cvt_pk_f16_f32 v105, v122, v123
	global_store_dwordx4 v[118:119], v[98:101], off
	global_store_dwordx4 v[118:119], v[102:105], off offset:256
	s_nop 0
	v_or_b32_e32 v100, 48, v148
	v_lshlrev_b64 v[102:103], 11, v[116:117]
	v_and_or_b32 v104, v100, s47, v166
	v_lshl_add_u64 v[102:103], v[146:147], 0, v[102:103]
	v_ashrrev_i32_e32 v105, 31, v104
	v_lshl_add_u64 v[104:105], v[104:105], 2, s[72:73]
	v_ashrrev_i32_e32 v101, 31, v100
	s_nop 0
	v_mov_b32_e32 v98, v228
	v_pk_mul_f32 v[96:97], v[96:97], v[98:99] op_sel_hi:[1,0]
	v_pk_mul_f32 v[94:95], v[94:95], v[98:99] op_sel_hi:[1,0]
	v_pk_mul_f32 v[92:93], v[92:93], v[98:99] op_sel_hi:[1,0]
	v_pk_mul_f32 v[90:91], v[90:91], v[98:99] op_sel_hi:[1,0]
	v_pk_mul_f32 v[88:89], v[88:89], v[98:99] op_sel_hi:[1,0]
	v_pk_mul_f32 v[86:87], v[86:87], v[98:99] op_sel_hi:[1,0]
	v_pk_mul_f32 v[106:107], v[84:85], v[98:99] op_sel_hi:[1,0]
	v_pk_mul_f32 v[98:99], v[82:83], v[98:99] op_sel_hi:[1,0]
	v_cvt_pk_f16_f32 v82, v94, v95
	v_cvt_pk_f16_f32 v83, v96, v97
	v_cvt_pk_f16_f32 v84, v90, v91
	v_cvt_pk_f16_f32 v85, v92, v93
	v_cvt_pk_f16_f32 v86, v86, v87
	v_cvt_pk_f16_f32 v87, v88, v89
	v_cvt_pk_f16_f32 v88, v98, v99
	v_cvt_pk_f16_f32 v89, v106, v107
	global_store_dwordx4 v[102:103], v[82:85], off
	global_store_dwordx4 v[102:103], v[86:89], off offset:256
	s_nop 0
	v_add_u32_e32 v84, 0x80, v148
	v_lshrrev_b32_e32 v83, 4, v84
	v_and_b32_e32 v83, 0xfffff0, v83
	v_add_lshl_u32 v92, v83, s16, 8
	v_lshlrev_b64 v[86:87], 11, v[100:101]
	v_and_or_b32 v88, v84, s38, v92
	v_lshl_add_u64 v[86:87], v[146:147], 0, v[86:87]
	v_ashrrev_i32_e32 v89, 31, v88
	v_lshl_add_u64 v[88:89], v[88:89], 2, s[72:73]
	v_ashrrev_i32_e32 v85, 31, v84
	s_nop 0
	v_mov_b32_e32 v82, v229
	v_pk_mul_f32 v[80:81], v[80:81], v[82:83] op_sel_hi:[1,0]
	v_pk_mul_f32 v[78:79], v[78:79], v[82:83] op_sel_hi:[1,0]
; #define GM_BAR __builtin_amdgcn_s_barrier()
;     __device__ __forceinline__ void operator()(const Acc& acc, const Unit& u, int wr, int wc, int fr, int fq) const {
;     ...
;             for (int m = 0; m < 4; ++m) { const int row = row0 + ai * HALF + m * 16; const float s = gv[((row >> 8) * NE + u.g) * CAP + (row & 255)];
;                 f16* rowp = Og + (size_t)row * DM + col0;
; #pragma unroll
;                 for (int bj = 0; bj < 2; ++bj) { const f32x4 v0 = acc[ai][bj][m][0] * s, v1 = acc[ai][bj][m][1] * s;
;                     u32x4 w; w.x = pkh(v0[0], v0[1]); w.y = pkh(v0[2], v0[3]); w.z = pkh(v1[0], v1[1]); w.w = pkh(v1[2], v1[3]);
;                     *(u32x4*)(rowp + bj * HALF) = w; } }
; template <bool BF, bool GATHER = false, class Epi, class Hook>
; __device__ __forceinline__ void gemm_phase(LAS unsigned char* lds, const Gemm g, const Order& S, const Epi& E, Hook& HK) {
;     ...
;         if (!has_next) break;
; #pragma unroll
;         for (int a = 0; a < 2; ++a)
; #pragma unroll
;             for (int b = 0; b < 2; ++b)
; #pragma unroll
;                 for (int m = 0; m < 4; ++m)
; #pragma unroll
;                     for (int n = 0; n < 2; ++n) acc[a][b][m][n] = (f32x4){0.f, 0.f, 0.f, 0.f};
;         cur = nxt; cA = nA; cB = nB; ++ui;
;         if constexpr (GATHER) { gA0[0] = nA0[0]; gA0[1] = nA0[1]; gA1[0] = nA1[0]; gA1[1] = nA1[1]; }
;         if (wr == 1) GM_BAR;
	v_pk_mul_f32 v[76:77], v[76:77], v[82:83] op_sel_hi:[1,0]
	v_pk_mul_f32 v[74:75], v[74:75], v[82:83] op_sel_hi:[1,0]
	v_pk_mul_f32 v[72:73], v[72:73], v[82:83] op_sel_hi:[1,0]
	v_pk_mul_f32 v[70:71], v[70:71], v[82:83] op_sel_hi:[1,0]
	v_pk_mul_f32 v[90:91], v[68:69], v[82:83] op_sel_hi:[1,0]
	v_pk_mul_f32 v[82:83], v[66:67], v[82:83] op_sel_hi:[1,0]
	v_cvt_pk_f16_f32 v66, v78, v79
	v_cvt_pk_f16_f32 v67, v80, v81
	v_cvt_pk_f16_f32 v68, v74, v75
	v_cvt_pk_f16_f32 v69, v76, v77
	v_cvt_pk_f16_f32 v70, v70, v71
	v_cvt_pk_f16_f32 v71, v72, v73
	v_cvt_pk_f16_f32 v72, v82, v83
	v_cvt_pk_f16_f32 v73, v90, v91
	global_store_dwordx4 v[86:87], v[66:69], off
	global_store_dwordx4 v[86:87], v[70:73], off offset:256
	s_nop 0
	v_add_u32_e32 v68, 0x90, v148
	v_lshlrev_b64 v[70:71], 11, v[84:85]
	v_and_or_b32 v72, v68, s45, v92
	v_lshl_add_u64 v[70:71], v[146:147], 0, v[70:71]
	v_ashrrev_i32_e32 v73, 31, v72
	v_lshl_add_u64 v[72:73], v[72:73], 2, s[72:73]
	v_ashrrev_i32_e32 v69, 31, v68
	s_nop 0
	v_mov_b32_e32 v66, v230
	v_pk_mul_f32 v[64:65], v[64:65], v[66:67] op_sel_hi:[1,0]
	v_pk_mul_f32 v[62:63], v[62:63], v[66:67] op_sel_hi:[1,0]
	v_pk_mul_f32 v[60:61], v[60:61], v[66:67] op_sel_hi:[1,0]
	v_pk_mul_f32 v[58:59], v[58:59], v[66:67] op_sel_hi:[1,0]
	v_pk_mul_f32 v[56:57], v[56:57], v[66:67] op_sel_hi:[1,0]
	v_pk_mul_f32 v[54:55], v[54:55], v[66:67] op_sel_hi:[1,0]
	v_pk_mul_f32 v[74:75], v[52:53], v[66:67] op_sel_hi:[1,0]
	v_pk_mul_f32 v[66:67], v[50:51], v[66:67] op_sel_hi:[1,0]
	v_cvt_pk_f16_f32 v50, v62, v63
	v_cvt_pk_f16_f32 v51, v64, v65
	v_cvt_pk_f16_f32 v52, v58, v59
	v_cvt_pk_f16_f32 v53, v60, v61
	v_cvt_pk_f16_f32 v54, v54, v55
	v_cvt_pk_f16_f32 v55, v56, v57
	v_cvt_pk_f16_f32 v56, v66, v67
	v_cvt_pk_f16_f32 v57, v74, v75
	global_store_dwordx4 v[70:71], v[50:53], off
	global_store_dwordx4 v[70:71], v[54:57], off offset:256
	s_nop 0
	v_add_u32_e32 v52, 0xa0, v148
	v_lshlrev_b64 v[54:55], 11, v[68:69]
	v_and_or_b32 v56, v52, s46, v92
	v_lshl_add_u64 v[54:55], v[146:147], 0, v[54:55]
	v_ashrrev_i32_e32 v57, 31, v56
	v_lshl_add_u64 v[56:57], v[56:57], 2, s[72:73]
	v_ashrrev_i32_e32 v53, 31, v52
	s_nop 0
	v_mov_b32_e32 v50, v231
	v_pk_mul_f32 v[48:49], v[48:49], v[50:51] op_sel_hi:[1,0]
	v_pk_mul_f32 v[46:47], v[46:47], v[50:51] op_sel_hi:[1,0]
	v_pk_mul_f32 v[44:45], v[44:45], v[50:51] op_sel_hi:[1,0]
	v_pk_mul_f32 v[42:43], v[42:43], v[50:51] op_sel_hi:[1,0]
	v_pk_mul_f32 v[40:41], v[40:41], v[50:51] op_sel_hi:[1,0]
	v_pk_mul_f32 v[38:39], v[38:39], v[50:51] op_sel_hi:[1,0]
	v_pk_mul_f32 v[58:59], v[36:37], v[50:51] op_sel_hi:[1,0]
	v_pk_mul_f32 v[50:51], v[34:35], v[50:51] op_sel_hi:[1,0]
	v_cvt_pk_f16_f32 v34, v46, v47
	v_cvt_pk_f16_f32 v35, v48, v49
	v_cvt_pk_f16_f32 v36, v42, v43
	v_cvt_pk_f16_f32 v37, v44, v45
	v_cvt_pk_f16_f32 v38, v38, v39
	v_cvt_pk_f16_f32 v39, v40, v41
	v_cvt_pk_f16_f32 v40, v50, v51
	v_cvt_pk_f16_f32 v41, v58, v59
	global_store_dwordx4 v[54:55], v[34:37], off
	global_store_dwordx4 v[54:55], v[38:41], off offset:256
	s_nop 0
	v_add_u32_e32 v36, 0xb0, v148
	v_lshlrev_b64 v[38:39], 11, v[52:53]
	v_and_or_b32 v40, v36, s47, v92
	v_lshl_add_u64 v[38:39], v[146:147], 0, v[38:39]
	v_ashrrev_i32_e32 v41, 31, v40
	v_lshl_add_u64 v[40:41], v[40:41], 2, s[72:73]
	v_ashrrev_i32_e32 v37, 31, v36
	s_nop 0
	v_mov_b32_e32 v34, v232
	v_pk_mul_f32 v[32:33], v[32:33], v[34:35] op_sel_hi:[1,0]
	v_pk_mul_f32 v[30:31], v[30:31], v[34:35] op_sel_hi:[1,0]
	v_pk_mul_f32 v[28:29], v[28:29], v[34:35] op_sel_hi:[1,0]
	v_pk_mul_f32 v[26:27], v[26:27], v[34:35] op_sel_hi:[1,0]
	v_pk_mul_f32 v[24:25], v[24:25], v[34:35] op_sel_hi:[1,0]
	v_pk_mul_f32 v[22:23], v[22:23], v[34:35] op_sel_hi:[1,0]
	v_pk_mul_f32 v[42:43], v[20:21], v[34:35] op_sel_hi:[1,0]
	v_pk_mul_f32 v[34:35], v[18:19], v[34:35] op_sel_hi:[1,0]
	v_cvt_pk_f16_f32 v18, v30, v31
	v_cvt_pk_f16_f32 v19, v32, v33
	v_cvt_pk_f16_f32 v20, v26, v27
	v_cvt_pk_f16_f32 v21, v28, v29
	v_cvt_pk_f16_f32 v22, v22, v23
	v_cvt_pk_f16_f32 v23, v24, v25
	v_cvt_pk_f16_f32 v24, v34, v35
	v_cvt_pk_f16_f32 v25, v42, v43
	global_store_dwordx4 v[38:39], v[18:21], off
	global_store_dwordx4 v[38:39], v[22:25], off offset:256
	s_nop 0
	v_lshlrev_b64 v[20:21], 11, v[36:37]
	v_lshl_add_u64 v[20:21], v[146:147], 0, v[20:21]
	s_nop 0
	v_mov_b32_e32 v18, v233
	v_pk_mul_f32 v[16:17], v[16:17], v[18:19] op_sel_hi:[1,0]
	v_pk_mul_f32 v[14:15], v[14:15], v[18:19] op_sel_hi:[1,0]
	v_pk_mul_f32 v[12:13], v[12:13], v[18:19] op_sel_hi:[1,0]
	v_pk_mul_f32 v[10:11], v[10:11], v[18:19] op_sel_hi:[1,0]
	v_pk_mul_f32 v[8:9], v[8:9], v[18:19] op_sel_hi:[1,0]
	v_pk_mul_f32 v[6:7], v[6:7], v[18:19] op_sel_hi:[1,0]
	v_pk_mul_f32 v[22:23], v[4:5], v[18:19] op_sel_hi:[1,0]
	v_pk_mul_f32 v[18:19], v[2:3], v[18:19] op_sel_hi:[1,0]
	v_cvt_pk_f16_f32 v2, v14, v15
	v_cvt_pk_f16_f32 v3, v16, v17
	v_cvt_pk_f16_f32 v4, v10, v11
	v_cvt_pk_f16_f32 v5, v12, v13
	v_cvt_pk_f16_f32 v6, v6, v7
	v_cvt_pk_f16_f32 v7, v8, v9
	v_cvt_pk_f16_f32 v8, v18, v19
	v_cvt_pk_f16_f32 v9, v22, v23
	global_store_dwordx4 v[20:21], v[2:5], off
	global_store_dwordx4 v[20:21], v[6:9], off offset:256
	s_cbranch_vccnz .LBB0_1852
	s_andn2_b64 vcc, exec, s[10:11]
	s_cbranch_vccnz .LBB0_1851
	s_barrier
	s_branch .LBB0_1851
